# speedup vs baseline: 1.0509x; 1.0509x over previous
.LBB2_24:
	s_cmp_lg_u32 s40, 0
	s_cselect_b64 s[4:5], -1, 0
	s_cmp_lg_u32 s62, s61
	s_cselect_b64 s[6:7], -1, 0
	s_or_b64 s[6:7], s[4:5], s[6:7]
	s_mov_b64 s[4:5], -1
	s_and_b64 vcc, exec, s[6:7]
	s_cbranch_vccz .LBB2_28
	v_div_scale_f32 v15, s[4:5], v14, v14, 1.0
	v_rcp_f32_e32 v17, v15
	v_mov_b32_e32 v33, v28
	s_load_dword s4, s[42:43], 0x1000
	v_mov_b32_e32 v67, v51
	v_fma_f32 v30, -v15, v17, 1.0
	v_fmac_f32_e32 v17, v30, v17
	v_div_scale_f32 v30, vcc, 1.0, v14, 1.0
	v_mul_f32_e32 v31, v30, v17
	v_fma_f32 v32, -v15, v31, v30
	v_fmac_f32_e32 v31, v32, v17
	v_fma_f32 v15, -v15, v31, v30
	v_div_fmas_f32 v15, v15, v17, v31
	v_div_fixup_f32 v15, v15, v14, 1.0
	v_cmp_lt_f32_e32 vcc, 0, v14
	v_mov_b32_e32 v32, v27
	s_waitcnt lgkmcnt(0)
	s_add_i32 s4, s4, s59
	v_cndmask_b32_e32 v30, 0, v15, vcc
	v_pk_mul_f32 v[32:33], v[30:31], v[32:33] op_sel_hi:[0,1]
	v_fma_mixlo_f16 v15, v30, v26, 0
	v_cvt_pk_f16_f32 v17, v32, v33
	v_pack_b32_f16 v32, v15, v17
	v_fma_mixlo_f16 v15, v30, v29, 0
	v_alignbit_b32 v33, v15, v17, 16
	ds_write_b64 v90, v[32:33] offset:32768
	v_mov_b32_e32 v32, v23
	v_mov_b32_e32 v33, v24
	v_pk_mul_f32 v[32:33], v[30:31], v[32:33] op_sel_hi:[0,1]
	v_fma_mixlo_f16 v15, v30, v22, 0
	v_cvt_pk_f16_f32 v17, v32, v33
	v_pack_b32_f16 v32, v15, v17
	v_fma_mixlo_f16 v15, v30, v25, 0
	v_alignbit_b32 v33, v15, v17, 16
	ds_write_b64 v91, v[32:33] offset:32768
	v_mov_b32_e32 v32, v19
	v_mov_b32_e32 v33, v20
	v_pk_mul_f32 v[32:33], v[30:31], v[32:33] op_sel_hi:[0,1]
	v_fma_mixlo_f16 v15, v30, v18, 0
	v_cvt_pk_f16_f32 v17, v32, v33
	v_pack_b32_f16 v32, v15, v17
	v_fma_mixlo_f16 v15, v30, v21, 0
	v_alignbit_b32 v33, v15, v17, 16
	ds_write_b64 v92, v[32:33] offset:32768
	v_mov_b32_e32 v32, v11
	v_mov_b32_e32 v33, v12
	v_pk_mul_f32 v[32:33], v[30:31], v[32:33] op_sel_hi:[0,1]
	v_fma_mixlo_f16 v15, v30, v10, 0
	v_cvt_pk_f16_f32 v17, v32, v33
	v_pack_b32_f16 v32, v15, v17
	v_fma_mixlo_f16 v15, v30, v13, 0
	v_alignbit_b32 v33, v15, v17, 16
	s_ashr_i32 s5, s4, 31
	ds_write_b64 v93, v[32:33] offset:32768
	s_lshl_b64 s[4:5], s[4:5], 7
	s_add_u32 s4, s4, s52
	s_waitcnt vmcnt(0)
	ds_read_b128 v[30:33], v94 offset:32768
	ds_read_b128 v[34:37], v95 offset:32768
	s_addc_u32 s5, s5, 0
	s_lshl_b64 s[6:7], s[4:5], 7
	v_lshl_add_u64 v[38:39], v[60:61], 0, s[6:7]
	v_lshl_add_u64 v[40:41], v[38:39], 0, v[50:51]
	s_waitcnt lgkmcnt(1)
	global_store_dwordx4 v[40:41], v[30:33], off sc1
	s_nop 1
	v_lshl_add_u64 v[30:31], v[38:39], 0, v[66:67]
	s_waitcnt lgkmcnt(0)
	global_store_dwordx4 v[30:31], v[34:37], off sc1
	s_and_saveexec_b64 s[6:7], s[0:1]
	s_cbranch_execz .LBB2_27
	v_mov_b32_e32 v31, s5
	v_or_b32_e32 v30, s4, v56
	v_lshl_add_u64 v[30:31], v[30:31], 3, s[44:45]
	v_mov_b32_e32 v17, v14
	global_store_dwordx2 v[30:31], v[16:17], off sc1

.LBB2_28:
	s_andn2_b64 vcc, exec, s[4:5]
	s_cbranch_vccnz .LBB2_2
	v_div_scale_f32 v15, s[4:5], v14, v14, 1.0
	v_rcp_f32_e32 v16, v15
	v_div_scale_f32 v17, vcc, 1.0, v14, 1.0
	s_add_i32 s40, s54, s60
	v_fma_f32 v30, -v15, v16, 1.0
	v_fmac_f32_e32 v16, v30, v16
	v_mul_f32_e32 v30, v17, v16
	v_fma_f32 v31, -v15, v30, v17
	v_fmac_f32_e32 v30, v31, v16
	v_fma_f32 v15, -v15, v30, v17
	v_div_fmas_f32 v15, v15, v16, v30
	v_div_fixup_f32 v30, v15, v14, 1.0
	v_pk_mul_f32 v[16:17], v[30:31], v[28:29] op_sel_hi:[0,1]
	v_pk_mul_f32 v[14:15], v[30:31], v[26:27] op_sel_hi:[0,1]
	v_add_u32_e32 v26, v85, v86
	ds_write_b128 v26, v[14:17] offset:32768
	v_pk_mul_f32 v[16:17], v[30:31], v[24:25] op_sel_hi:[0,1]
	v_pk_mul_f32 v[14:15], v[30:31], v[22:23] op_sel_hi:[0,1]
	v_add_u32_e32 v22, v85, v87
	ds_write_b128 v22, v[14:17] offset:32768
	v_pk_mul_f32 v[16:17], v[30:31], v[20:21] op_sel_hi:[0,1]
	v_pk_mul_f32 v[14:15], v[30:31], v[18:19] op_sel_hi:[0,1]
	v_add_u32_e32 v18, v85, v88
	ds_write_b128 v18, v[14:17] offset:32768
	v_pk_mul_f32 v[12:13], v[30:31], v[12:13] op_sel_hi:[0,1]
	v_pk_mul_f32 v[10:11], v[30:31], v[10:11] op_sel_hi:[0,1]
	v_add_u32_e32 v14, v85, v89
	ds_write_b128 v14, v[10:13] offset:32768
	ds_read_b128 v[10:13], v96 offset:32768
	ds_read_b128 v[14:17], v97 offset:32768
	s_lshl_b64 s[4:5], s[40:41], 8
	v_lshl_add_u64 v[18:19], v[62:63], 0, s[4:5]
	v_mov_b32_e32 v69, v51
	v_lshl_add_u64 v[20:21], v[18:19], 0, v[68:69]
	v_mov_b32_e32 v71, v51
	s_waitcnt lgkmcnt(0)
	global_store_dwordx4 v[20:21], v[10:13], off sc1
	v_lshl_add_u64 v[20:21], v[18:19], 0, v[70:71]
	ds_read_b128 v[10:13], v98 offset:32768
	global_store_dwordx4 v[20:21], v[14:17], off sc1
	ds_read_b128 v[14:17], v99 offset:32768
	v_mov_b32_e32 v73, v51
	v_lshl_add_u64 v[20:21], v[18:19], 0, v[72:73]
	v_mov_b32_e32 v75, v51
	s_waitcnt lgkmcnt(0)
	global_store_dwordx4 v[20:21], v[10:13], off sc1
	s_nop 1
	v_lshl_add_u64 v[10:11], v[18:19], 0, v[74:75]
	global_store_dwordx4 v[10:11], v[14:17], off sc1
	s_branch .LBB2_2
